# speedup vs baseline: 1.0027x; 1.0027x over previous
.LBB1_8:
	s_or_b64 exec, exec, s[4:5]
	v_add_u32_e32 v10, v172, v2
	s_waitcnt vmcnt(1) lgkmcnt(0)
	s_barrier
	s_nop 0
	s_nop 0
	s_nop 0
	s_nop 0
	ds_read_b128 v[18:21], v10 offset:256
	ds_read_b128 v[22:25], v10 offset:288
	ds_read_b128 v[82:85], v10 offset:320
	ds_read_b128 v[86:89], v10 offset:352
	ds_read_b128 v[74:77], v10 offset:384
	ds_read_b128 v[78:81], v10 offset:416
	ds_read_b128 v[2:5], v213 offset:32768
	ds_read_b128 v[6:9], v213 offset:0
	ds_read_b128 v[66:69], v10 offset:448
	ds_read_b128 v[70:73], v10 offset:480
	ds_read_b128 v[10:13], v213 offset:1024
	s_waitcnt lgkmcnt(3)
	v_pk_mul_f32 v[26:27], v[8:9], v[20:21]
	v_pk_mul_f32 v[28:29], v[6:7], v[18:19]
	ds_read_b128 v[14:17], v213 offset:8192
	s_waitcnt lgkmcnt(1)
	v_pk_mul_f32 v[12:13], v[12:13], v[24:25]
	v_pk_mul_f32 v[10:11], v[10:11], v[22:23]
	v_pk_fma_f32 v[30:31], v[8:9], v[20:21], v[12:13]
	v_pk_fma_f32 v[32:33], v[6:7], v[18:19], v[10:11]
	v_cvt_pk_bf16_f32 v9, v12, v13
	v_cvt_pk_bf16_f32 v7, v26, v27
	v_cvt_pk_bf16_f32 v8, v10, v11
	v_cvt_pk_bf16_f32 v6, v28, v29
	ds_read_b128 v[10:13], v213 offset:33792
	s_nop 0
	v_mfma_f32_32x32x16_bf16 v[34:49], v[2:5], v[6:9], 0
	ds_read_b128 v[6:9], v213 offset:9216
	s_waitcnt lgkmcnt(2)
	v_mul_f32_e32 v26, v16, v20
	v_mul_f32_e32 v27, v17, v21
	v_pk_mul_f32 v[50:51], v[14:15], v[18:19]
	s_mov_b32 s4, 0x3727c5ac
	s_waitcnt lgkmcnt(0)
	v_pk_mul_f32 v[8:9], v[8:9], v[24:25]
	v_pk_mul_f32 v[28:29], v[6:7], v[22:23]
	v_pk_fma_f32 v[90:91], v[16:17], v[20:21], v[8:9]
	v_pk_fma_f32 v[92:93], v[14:15], v[18:19], v[28:29]
	ds_read_b128 v[14:17], v213 offset:2048
	v_cvt_pk_bf16_f32 v9, v8, v9
	v_cvt_pk_bf16_f32 v7, v26, v27
	v_cvt_pk_bf16_f32 v8, v28, v29
	ds_read_b128 v[26:29], v213 offset:3072
	v_cvt_pk_bf16_f32 v6, v50, v51
	s_waitcnt lgkmcnt(1)
	v_pk_mul_f32 v[94:95], v[14:15], v[82:83]
	s_mov_b32 s0, 0x3c800000
	v_mfma_f32_32x32x16_bf16 v[50:65], v[2:5], v[6:9], 0
	v_mul_f32_e32 v2, v16, v84
	v_mul_f32_e32 v3, v17, v85
	s_waitcnt lgkmcnt(0)
	v_mul_f32_e32 v4, v28, v88
	v_mul_f32_e32 v5, v29, v89
	v_pk_mul_f32 v[6:7], v[26:27], v[86:87]
	v_pk_fma_f32 v[8:9], v[16:17], v[84:85], v[4:5]
	v_cvt_pk_bf16_f32 v3, v2, v3
	v_pk_fma_f32 v[14:15], v[14:15], v[82:83], v[6:7]
	v_pk_add_f32 v[26:27], v[8:9], v[30:31]
	v_cvt_pk_bf16_f32 v5, v4, v5
	v_cvt_pk_bf16_f32 v4, v6, v7
	ds_read_b128 v[6:9], v213 offset:10240
	v_pk_add_f32 v[28:29], v[14:15], v[32:33]
	ds_read_b128 v[14:17], v213 offset:11264
	v_cvt_pk_bf16_f32 v2, v94, v95
	s_waitcnt lgkmcnt(1)
	v_pk_mul_f32 v[30:31], v[6:7], v[82:83]
	v_mov_b64_e32 v[152:153], s[4:5]
	v_mfma_f32_32x32x16_bf16 v[34:49], v[10:13], v[2:5], v[34:49]
	v_mul_f32_e32 v2, v8, v84
	v_mul_f32_e32 v3, v9, v85
	s_waitcnt lgkmcnt(0)
	v_mul_f32_e32 v4, v16, v88
	v_mul_f32_e32 v5, v17, v89
	v_pk_mul_f32 v[14:15], v[14:15], v[86:87]
	v_pk_fma_f32 v[8:9], v[8:9], v[84:85], v[4:5]
	v_pk_fma_f32 v[6:7], v[6:7], v[82:83], v[14:15]
	v_cvt_pk_bf16_f32 v5, v4, v5
	v_cvt_pk_bf16_f32 v3, v2, v3
	v_cvt_pk_bf16_f32 v4, v14, v15
	v_pk_add_f32 v[32:33], v[8:9], v[90:91]
	v_pk_add_f32 v[90:91], v[6:7], v[92:93]
	ds_read_b128 v[6:9], v213 offset:34816
	ds_read_b128 v[14:17], v213 offset:4096
	v_cvt_pk_bf16_f32 v2, v30, v31
	s_mov_b32 s13, 0
	s_mov_b64 s[6:7], 0
	v_mfma_f32_32x32x16_bf16 v[50:65], v[10:13], v[2:5], v[50:65]
	ds_read_b128 v[2:5], v213 offset:5120
	ds_read_b128 v[10:13], v213 offset:12288
	s_waitcnt lgkmcnt(2)
	v_pk_mul_f32 v[30:31], v[16:17], v[76:77]
	v_pk_mul_f32 v[92:93], v[14:15], v[74:75]
	s_waitcnt lgkmcnt(1)
	v_pk_mul_f32 v[4:5], v[4:5], v[80:81]
	v_pk_mul_f32 v[94:95], v[2:3], v[78:79]
	v_pk_fma_f32 v[2:3], v[16:17], v[76:77], v[4:5]
	v_cvt_pk_bf16_f32 v5, v4, v5
	v_pk_add_f32 v[96:97], v[2:3], v[26:27]
	v_cvt_pk_bf16_f32 v3, v30, v31
	v_cvt_pk_bf16_f32 v4, v94, v95
	v_cvt_pk_bf16_f32 v2, v92, v93
	v_pk_fma_f32 v[14:15], v[14:15], v[74:75], v[94:95]
	s_waitcnt lgkmcnt(0)
	v_pk_mul_f32 v[30:31], v[10:11], v[74:75]
	v_mfma_f32_32x32x16_bf16 v[34:49], v[6:9], v[2:5], v[34:49]
	ds_read_b128 v[2:5], v213 offset:13312
	v_add_f32_e32 v98, v14, v28
	v_add_f32_e32 v99, v15, v29
	ds_read_b128 v[14:17], v213 offset:35840
	v_pk_mul_f32 v[26:27], v[12:13], v[76:77]
	s_waitcnt lgkmcnt(1)
	v_pk_mul_f32 v[4:5], v[4:5], v[80:81]
	v_pk_mul_f32 v[28:29], v[2:3], v[78:79]
	v_pk_fma_f32 v[2:3], v[12:13], v[76:77], v[4:5]
	v_pk_fma_f32 v[10:11], v[10:11], v[74:75], v[28:29]
	v_pk_add_f32 v[32:33], v[2:3], v[32:33]
	v_pk_add_f32 v[92:93], v[10:11], v[90:91]
	ds_read_b128 v[10:13], v213 offset:6144
	v_cvt_pk_bf16_f32 v5, v4, v5
	v_cvt_pk_bf16_f32 v3, v26, v27
	v_cvt_pk_bf16_f32 v4, v28, v29
	ds_read_b128 v[26:29], v213 offset:7168
	v_cvt_pk_bf16_f32 v2, v30, v31
	s_waitcnt lgkmcnt(1)
	v_pk_mul_f32 v[30:31], v[10:11], v[66:67]
	v_mfma_f32_32x32x16_bf16 v[50:65], v[6:9], v[2:5], v[50:65]
	v_mul_f32_e32 v2, v12, v68
	v_mul_f32_e32 v3, v13, v69
	s_waitcnt lgkmcnt(0)
	v_mul_f32_e32 v4, v28, v72
	v_mul_f32_e32 v5, v29, v73
	v_pk_mul_f32 v[6:7], v[26:27], v[70:71]
	v_pk_fma_f32 v[8:9], v[12:13], v[68:69], v[4:5]
	v_cvt_pk_bf16_f32 v3, v2, v3
	v_pk_fma_f32 v[10:11], v[10:11], v[66:67], v[6:7]
	v_pk_add_f32 v[94:95], v[8:9], v[96:97]
	v_cvt_pk_bf16_f32 v5, v4, v5
	v_cvt_pk_bf16_f32 v4, v6, v7
	ds_read_b128 v[6:9], v213 offset:14336
	v_pk_add_f32 v[96:97], v[10:11], v[98:99]
	ds_read_b128 v[10:13], v213 offset:15360
	v_cvt_pk_bf16_f32 v2, v30, v31
	s_waitcnt lgkmcnt(1)
	v_pk_mul_f32 v[30:31], v[6:7], v[66:67]
	v_mfma_f32_32x32x16_bf16 v[34:49], v[14:17], v[2:5], v[34:49]
	s_waitcnt lgkmcnt(0)
	v_mul_f32_e32 v10, v10, v70
	v_mul_f32_e32 v11, v11, v71
	v_mul_f32_e32 v2, v8, v68
	v_mul_f32_e32 v3, v9, v69
	v_pk_mul_f32 v[4:5], v[12:13], v[72:73]
	v_pk_fma_f32 v[6:7], v[6:7], v[66:67], v[10:11]
	v_pk_fma_f32 v[8:9], v[8:9], v[68:69], v[4:5]
	v_pk_add_f32 v[92:93], v[6:7], v[92:93]
	v_cvt_pk_bf16_f32 v3, v2, v3
	v_pk_add_f32 v[90:91], v[8:9], v[32:33]
	v_cvt_pk_bf16_f32 v5, v4, v5
	v_cvt_pk_bf16_f32 v4, v10, v11
	ds_read_b128 v[26:29], v213 offset:36864
	ds_read_b128 v[6:9], v213 offset:16384
	v_cvt_pk_bf16_f32 v2, v30, v31
	ds_read_b128 v[98:101], v213 offset:25600
	ds_read_b128 v[102:105], v213 offset:37888
	v_mfma_f32_32x32x16_bf16 v[50:65], v[14:17], v[2:5], v[50:65]
	ds_read_b128 v[2:5], v213 offset:17408
	ds_read_b128 v[30:33], v213 offset:24576
	s_waitcnt lgkmcnt(4)
	v_pk_mul_f32 v[12:13], v[6:7], v[18:19]
	v_pk_mul_f32 v[10:11], v[8:9], v[20:21]
	s_waitcnt lgkmcnt(1)
	v_pk_mul_f32 v[14:15], v[2:3], v[22:23]
	v_pk_mul_f32 v[22:23], v[98:99], v[22:23]
	v_pk_fma_f32 v[112:113], v[6:7], v[18:19], v[14:15]
	s_waitcnt lgkmcnt(0)
	v_pk_mul_f32 v[114:115], v[30:31], v[18:19]
	v_pk_fma_f32 v[118:119], v[30:31], v[18:19], v[22:23]
	v_pk_mul_f32 v[4:5], v[4:5], v[24:25]
	v_pk_mul_f32 v[106:107], v[32:33], v[20:21]
	v_pk_mul_f32 v[24:25], v[100:101], v[24:25]
	ds_read_b128 v[98:101], v213 offset:18432
	v_cvt_pk_bf16_f32 v19, v106, v107
	ds_read_b128 v[106:109], v213 offset:19456
	v_pk_fma_f32 v[110:111], v[8:9], v[20:21], v[4:5]
	v_cvt_pk_bf16_f32 v5, v4, v5
	v_cvt_pk_bf16_f32 v3, v10, v11
	v_cvt_pk_bf16_f32 v4, v14, v15
	s_waitcnt lgkmcnt(0)
	v_pk_mul_f32 v[106:107], v[106:107], v[86:87]
	v_cvt_pk_bf16_f32 v2, v12, v13
	v_pk_mul_f32 v[120:121], v[98:99], v[82:83]
	v_pk_mul_f32 v[108:109], v[108:109], v[88:89]
	v_pk_fma_f32 v[98:99], v[98:99], v[82:83], v[106:107]
	v_mfma_f32_32x32x16_bf16 v[2:17], v[26:29], v[2:5], 0
	v_cvt_pk_bf16_f32 v18, v114, v115
	v_mul_f32_e32 v114, v100, v84
	v_mul_f32_e32 v115, v101, v85
	v_fma_f32 v100, v100, v84, v108
	v_fma_f32 v101, v101, v85, v109
	v_pk_add_f32 v[124:125], v[98:99], v[112:113]
	v_pk_add_f32 v[122:123], v[100:101], v[110:111]
	v_cvt_pk_bf16_f32 v101, v108, v109
	v_cvt_pk_bf16_f32 v100, v106, v107
	ds_read_b128 v[106:109], v213 offset:26624
	v_pk_fma_f32 v[116:117], v[32:33], v[20:21], v[24:25]
	v_cvt_pk_bf16_f32 v21, v24, v25
	v_cvt_pk_bf16_f32 v20, v22, v23
	ds_read_b128 v[110:113], v213 offset:27648
	v_cvt_pk_bf16_f32 v99, v114, v115
	v_mfma_f32_32x32x16_bf16 v[18:33], v[26:29], v[18:21], 0
	v_cvt_pk_bf16_f32 v98, v120, v121
	s_waitcnt lgkmcnt(1)
	v_mul_f32_e32 v114, v106, v82
	v_mul_f32_e32 v115, v107, v83
	s_waitcnt lgkmcnt(0)
	v_pk_mul_f32 v[86:87], v[110:111], v[86:87]
	v_pk_mul_f32 v[88:89], v[112:113], v[88:89]
	v_pk_fma_f32 v[82:83], v[106:107], v[82:83], v[86:87]
	v_mfma_f32_32x32x16_bf16 v[2:17], v[102:105], v[98:101], v[2:17]
	v_mul_f32_e32 v98, v108, v84
	v_mul_f32_e32 v99, v109, v85
	v_fma_f32 v84, v108, v84, v88
	v_fma_f32 v85, v109, v85, v89
	v_add_f32_e32 v108, v82, v118
	v_add_f32_e32 v109, v83, v119
	v_cvt_pk_bf16_f32 v83, v98, v99
	v_pk_add_f32 v[106:107], v[84:85], v[116:117]
	v_cvt_pk_bf16_f32 v85, v88, v89
	v_cvt_pk_bf16_f32 v84, v86, v87
	ds_read_b128 v[86:89], v213 offset:38912
	ds_read_b128 v[98:101], v213 offset:20480
	v_cvt_pk_bf16_f32 v82, v114, v115
	s_waitcnt lgkmcnt(0)
	v_pk_mul_f32 v[110:111], v[100:101], v[76:77]
	v_mfma_f32_32x32x16_bf16 v[18:33], v[102:105], v[82:85], v[18:33]
	ds_read_b128 v[82:85], v213 offset:21504
	ds_read_b128 v[102:105], v213 offset:28672
	v_mul_f32_e32 v112, v98, v74
	v_mul_f32_e32 v113, v99, v75
	s_waitcnt lgkmcnt(1)
	v_pk_mul_f32 v[84:85], v[84:85], v[80:81]
	v_pk_mul_f32 v[114:115], v[82:83], v[78:79]
	v_pk_fma_f32 v[82:83], v[100:101], v[76:77], v[84:85]
	v_cvt_pk_bf16_f32 v85, v84, v85
	v_pk_add_f32 v[116:117], v[82:83], v[122:123]
	v_cvt_pk_bf16_f32 v83, v110, v111
	v_cvt_pk_bf16_f32 v84, v114, v115
	v_cvt_pk_bf16_f32 v82, v112, v113
	v_pk_fma_f32 v[98:99], v[98:99], v[74:75], v[114:115]
	s_waitcnt lgkmcnt(0)
	v_pk_mul_f32 v[112:113], v[102:103], v[74:75]
	v_mfma_f32_32x32x16_bf16 v[2:17], v[86:89], v[82:85], v[2:17]
	ds_read_b128 v[82:85], v213 offset:29696
	v_add_f32_e32 v118, v98, v124
	v_add_f32_e32 v119, v99, v125
	v_mul_f32_e32 v110, v104, v76
	v_mul_f32_e32 v111, v105, v77
	ds_read_b128 v[98:101], v213 offset:39936
	s_waitcnt lgkmcnt(1)
	v_pk_mul_f32 v[78:79], v[82:83], v[78:79]
	v_pk_mul_f32 v[80:81], v[84:85], v[80:81]
	v_pk_fma_f32 v[74:75], v[102:103], v[74:75], v[78:79]
	v_pk_fma_f32 v[76:77], v[104:105], v[76:77], v[80:81]
	v_pk_add_f32 v[104:105], v[74:75], v[108:109]
	v_pk_add_f32 v[102:103], v[76:77], v[106:107]
	v_cvt_pk_bf16_f32 v77, v80, v81
	v_cvt_pk_bf16_f32 v76, v78, v79
	ds_read_b128 v[78:81], v213 offset:22528
	ds_read_b128 v[82:85], v213 offset:23552
	v_cvt_pk_bf16_f32 v75, v110, v111
	v_cvt_pk_bf16_f32 v74, v112, v113
	s_waitcnt lgkmcnt(0)
	v_pk_mul_f32 v[82:83], v[82:83], v[70:71]
	v_mfma_f32_32x32x16_bf16 v[18:33], v[86:89], v[74:77], v[18:33]
	v_mul_f32_e32 v74, v80, v68
	v_mul_f32_e32 v75, v81, v69
	v_mul_f32_e32 v76, v84, v72
	v_mul_f32_e32 v77, v85, v73
	v_mul_f32_e32 v86, v78, v66
	v_mul_f32_e32 v87, v79, v67
	v_pk_fma_f32 v[80:81], v[80:81], v[68:69], v[76:77]
	v_pk_fma_f32 v[78:79], v[78:79], v[66:67], v[82:83]
	v_cvt_pk_bf16_f32 v75, v74, v75
	v_pk_add_f32 v[88:89], v[80:81], v[116:117]
	v_pk_add_f32 v[106:107], v[78:79], v[118:119]
	ds_read_b128 v[78:81], v213 offset:30720
	v_cvt_pk_bf16_f32 v77, v76, v77
	v_cvt_pk_bf16_f32 v76, v82, v83
	ds_read_b128 v[82:85], v213 offset:31744
	v_cvt_pk_bf16_f32 v74, v86, v87
	s_waitcnt lgkmcnt(0)
	v_pk_mul_f32 v[72:73], v[84:85], v[72:73]
	v_mfma_f32_32x32x16_bf16 v[2:17], v[98:101], v[74:77], v[2:17]
	v_mul_f32_e32 v74, v80, v68
	v_mul_f32_e32 v75, v81, v69
	v_fma_f32 v68, v80, v68, v72
	v_fma_f32 v69, v81, v69, v73
	v_mul_f32_e32 v70, v82, v70
	v_mul_f32_e32 v71, v83, v71
	v_pk_add_f32 v[84:85], v[68:69], v[102:103]
	v_cvt_pk_bf16_f32 v69, v72, v73
	v_pk_mov_b32 v[72:73], v[96:97], v[94:95] op_sel:[1,0]
	v_mov_b32_e32 v97, v95
	v_pk_add_f32 v[72:73], v[72:73], v[96:97]
	v_pk_mul_f32 v[76:77], v[78:79], v[66:67]
	v_pk_fma_f32 v[66:67], v[78:79], v[66:67], v[70:71]
	v_pk_add_f32 v[72:73], v[72:73], v[72:73] op_sel:[0,1] op_sel_hi:[1,0]
	v_pk_add_f32 v[86:87], v[66:67], v[104:105]
	v_mov_b32_e32 v66, v72
	s_nop 1
	v_permlane32_swap_b32_e32 v72, v66
	v_add_f32_e32 v66, v72, v66
	v_cvt_pk_bf16_f32 v67, v74, v75
	v_rcp_f32_e32 v74, v66
	v_cvt_pk_bf16_f32 v68, v70, v71
	v_cvt_pk_bf16_f32 v66, v76, v77
	v_pk_mul_f32 v[70:71], v[46:47], v[74:75] op_sel_hi:[1,0]
	s_nop 0
	v_mfma_f32_32x32x16_bf16 v[18:33], v[98:101], v[66:69], v[18:33]
	v_mul_f32_e32 v66, v42, v74
	v_mul_f32_e32 v67, v43, v74
	v_pk_mov_b32 v[42:43], v[92:93], v[90:91] op_sel:[1,0]
	v_mov_b32_e32 v93, v91
	v_pk_add_f32 v[42:43], v[42:43], v[92:93]
	v_pk_mul_f32 v[68:69], v[44:45], v[74:75] op_sel_hi:[1,0]
	v_pk_add_f32 v[42:43], v[42:43], v[42:43] op_sel:[0,1] op_sel_hi:[1,0]
	v_pk_mov_b32 v[44:45], v[106:107], v[88:89] op_sel:[1,0]
	v_mov_b32_e32 v43, v42
	s_nop 1
	v_permlane32_swap_b32_e32 v42, v43
	v_add_f32_e32 v42, v42, v43
	v_rcp_f32_e32 v42, v42
	v_mov_b32_e32 v107, v89
	v_pk_add_f32 v[44:45], v[44:45], v[106:107]
	v_pk_mul_f32 v[72:73], v[48:49], v[74:75] op_sel_hi:[1,0]
	v_pk_add_f32 v[44:45], v[44:45], v[44:45] op_sel:[0,1] op_sel_hi:[1,0]
	v_pk_mul_f32 v[36:37], v[36:37], v[74:75] op_sel_hi:[1,0]
	v_pk_mul_f32 v[38:39], v[38:39], v[74:75] op_sel_hi:[1,0]
	v_pk_mul_f32 v[40:41], v[40:41], v[74:75] op_sel_hi:[1,0]
	v_pk_mul_f32 v[34:35], v[34:35], v[74:75] op_sel_hi:[1,0]
	v_pk_mul_f32 v[74:75], v[58:59], v[42:43] op_sel_hi:[1,0]
	v_pk_mul_f32 v[78:79], v[60:61], v[42:43] op_sel_hi:[1,0]
	v_pk_mul_f32 v[80:81], v[62:63], v[42:43] op_sel_hi:[1,0]
	v_pk_mul_f32 v[82:83], v[64:65], v[42:43] op_sel_hi:[1,0]
	v_pk_mul_f32 v[92:93], v[52:53], v[42:43] op_sel_hi:[1,0]
	v_mov_b32_e32 v43, v44
	s_nop 1
	v_permlane32_swap_b32_e32 v44, v43
	v_add_f32_e32 v43, v44, v43
	v_rcp_f32_e32 v76, v43
	v_pk_mul_f32 v[96:97], v[54:55], v[42:43] op_sel_hi:[1,0]
	v_pk_mul_f32 v[94:95], v[56:57], v[42:43] op_sel_hi:[1,0]
	v_pk_mul_f32 v[98:99], v[50:51], v[42:43] op_sel_hi:[1,0]
	v_pk_mul_f32 v[100:101], v[4:5], v[76:77] op_sel_hi:[1,0]
	v_pk_mov_b32 v[4:5], v[86:87], v[84:85] op_sel:[1,0]
	v_mov_b32_e32 v87, v85
	v_pk_add_f32 v[4:5], v[4:5], v[86:87]
	v_pk_mul_f32 v[102:103], v[6:7], v[76:77] op_sel_hi:[1,0]
	v_pk_add_f32 v[104:105], v[4:5], v[4:5] op_sel:[0,1] op_sel_hi:[1,0]
	v_cvt_pk_bf16_f32 v7, v40, v41
	s_nop 0
	s_nop 0
	s_nop 0
	s_nop 0
	s_nop 0
	s_nop 0
	s_nop 0
	s_nop 0
	s_nop 0
	s_nop 0
	s_nop 0
	s_nop 0
	ds_read_b128 v[84:87], v150 offset:52224
	ds_read_b128 v[50:53], v150 offset:35840
	ds_read_b128 v[54:57], v150 offset:36864
	ds_read_b128 v[58:61], v150 offset:37888
	ds_read_b128 v[62:65], v150 offset:38912
	v_cvt_pk_bf16_f32 v6, v38, v39
	v_cvt_pk_bf16_f32 v5, v36, v37
	v_cvt_pk_bf16_f32 v4, v34, v35
	ds_read_b128 v[88:91], v150 offset:53248
	ds_read_b128 v[34:37], v150 offset:39936
	ds_read_b128 v[38:41], v150 offset:40960
	ds_read_b128 v[42:45], v150 offset:41984
	ds_read_b128 v[46:49], v150 offset:43008
	v_cvt_pk_bf16_f32 v95, v94, v95
	v_cvt_pk_bf16_f32 v94, v96, v97
	v_cvt_pk_bf16_f32 v93, v92, v93
	v_cvt_pk_bf16_f32 v92, v98, v99
	s_waitcnt lgkmcnt(5)
	v_mfma_f32_32x32x16_bf16 v[50:65], v[84:87], v[4:7], v[50:65]
	v_mul_f32_e32 v10, v10, v76
	v_mul_f32_e32 v11, v11, v76
	v_mul_f32_e32 v12, v12, v76
	v_mul_f32_e32 v13, v13, v76
	v_mul_f32_e32 v8, v8, v76
	v_mul_f32_e32 v9, v9, v76
	v_mov_b32_e32 v77, v104
	s_nop 1
	v_permlane32_swap_b32_e32 v104, v77
	v_cvt_pk_bf16_f32 v73, v72, v73
	s_waitcnt lgkmcnt(0)
	v_mfma_f32_32x32x16_bf16 v[34:49], v[84:87], v[92:95], v[34:49]
	v_cvt_pk_bf16_f32 v72, v70, v71
	v_cvt_pk_bf16_f32 v70, v66, v67
	v_add_f32_e32 v66, v104, v77
	v_cvt_pk_bf16_f32 v71, v68, v69
	v_rcp_f32_e32 v104, v66
	v_cvt_pk_bf16_f32 v69, v82, v83
	v_cvt_pk_bf16_f32 v68, v80, v81
	v_cvt_pk_bf16_f32 v67, v78, v79
	v_cvt_pk_bf16_f32 v66, v74, v75
	ds_read_b128 v[78:81], v150 offset:54272
	v_mfma_f32_32x32x16_bf16 v[50:65], v[88:91], v[70:73], v[50:65]
	v_mul_f32_e32 v2, v2, v76
	v_mul_f32_e32 v3, v3, v76
	v_mul_f32_e32 v20, v20, v104
	v_mul_f32_e32 v21, v21, v104
	v_cvt_pk_bf16_f32 v85, v8, v9
	v_cvt_pk_bf16_f32 v82, v2, v3
	v_pk_mul_f32 v[2:3], v[22:23], v[104:105] op_sel_hi:[1,0]
	v_pk_mul_f32 v[8:9], v[24:25], v[104:105] op_sel_hi:[1,0]
	v_pk_mul_f32 v[18:19], v[18:19], v[104:105] op_sel_hi:[1,0]
	v_mfma_f32_32x32x16_bf16 v[34:49], v[88:91], v[66:69], v[34:49]
	v_cvt_pk_bf16_f32 v84, v102, v103
	v_cvt_pk_bf16_f32 v83, v100, v101
	ds_read_b128 v[86:89], v150 offset:55296
	v_cvt_pk_bf16_f32 v99, v8, v9
	v_cvt_pk_bf16_f32 v98, v2, v3
	v_cvt_pk_bf16_f32 v97, v20, v21
	v_cvt_pk_bf16_f32 v96, v18, v19
	s_waitcnt lgkmcnt(1)
	v_mfma_f32_32x32x16_bf16 v[50:65], v[78:81], v[82:85], v[50:65]
	v_mul_f32_e32 v2, v14, v76
	v_mul_f32_e32 v3, v15, v76
	v_mul_f32_e32 v8, v16, v76
	v_mul_f32_e32 v9, v17, v76
	v_mul_f32_e32 v14, v26, v104
	v_mul_f32_e32 v15, v27, v104
	v_cvt_pk_bf16_f32 v77, v8, v9
	v_cvt_pk_bf16_f32 v76, v2, v3
	v_cvt_pk_bf16_f32 v74, v10, v11
	v_pk_mul_f32 v[2:3], v[28:29], v[104:105] op_sel_hi:[1,0]
	v_mfma_f32_32x32x16_bf16 v[34:49], v[78:81], v[96:99], v[34:49]
	v_mul_f32_e32 v8, v30, v104
	v_mul_f32_e32 v9, v31, v104
	v_mul_f32_e32 v10, v32, v104
	v_mul_f32_e32 v11, v33, v104
	v_cvt_pk_bf16_f32 v75, v12, v13
	v_cvt_pk_bf16_f32 v81, v10, v11
	v_cvt_pk_bf16_f32 v80, v8, v9
	v_cvt_pk_bf16_f32 v79, v2, v3
	v_cvt_pk_bf16_f32 v78, v14, v15
	s_waitcnt lgkmcnt(0)
	v_mfma_f32_32x32x16_bf16 v[50:65], v[86:89], v[74:77], v[50:65]
	v_mfma_f32_32x32x16_bf16 v[34:49], v[86:89], v[78:81], v[34:49]
	ds_read_b128 v[86:89], v150 offset:56320
	ds_read_b128 v[18:21], v150 offset:44032
	ds_read_b128 v[22:25], v150 offset:45056
	ds_read_b128 v[26:29], v150 offset:46080
	ds_read_b128 v[30:33], v150 offset:47104
	ds_read_b128 v[100:103], v150 offset:57344
	s_waitcnt lgkmcnt(1)
	v_mfma_f32_32x32x16_bf16 v[18:33], v[86:89], v[4:7], v[18:33]
	ds_read_b128 v[2:5], v150 offset:48128
	ds_read_b128 v[6:9], v150 offset:49152
	ds_read_b128 v[10:13], v150 offset:50176
	ds_read_b128 v[14:17], v150 offset:51200
	s_waitcnt lgkmcnt(0)
	v_mfma_f32_32x32x16_bf16 v[2:17], v[86:89], v[92:95], v[2:17]
	v_mfma_f32_32x32x16_bf16 v[18:33], v[100:103], v[70:73], v[18:33]
	v_mfma_f32_32x32x16_bf16 v[2:17], v[100:103], v[66:69], v[2:17]
	ds_read_b128 v[66:69], v150 offset:58368
	ds_read_b128 v[70:73], v150 offset:59392
	s_waitcnt lgkmcnt(1)
	v_mfma_f32_32x32x16_bf16 v[18:33], v[66:69], v[82:85], v[18:33]
	v_mfma_f32_32x32x16_bf16 v[2:17], v[66:69], v[96:99], v[2:17]
	s_waitcnt lgkmcnt(0)
	v_mfma_f32_32x32x16_bf16 v[18:33], v[70:73], v[74:77], v[18:33]
	v_mfma_f32_32x32x16_bf16 v[2:17], v[70:73], v[78:81], v[2:17]
	s_nop 10
	v_mul_f32_e32 v66, v22, v22
	v_mul_f32_e32 v67, v23, v23
	v_mul_f32_e32 v68, v30, v30
	v_mul_f32_e32 v69, v31, v31
	v_mul_f32_e32 v70, v24, v24
	v_mul_f32_e32 v71, v25, v25
	v_pk_mul_f32 v[72:73], v[32:33], v[32:33]
	v_pk_mul_f32 v[74:75], v[20:21], v[20:21]
	v_pk_mul_f32 v[76:77], v[28:29], v[28:29]
	v_pk_mul_f32 v[78:79], v[26:27], v[26:27]
	v_pk_mul_f32 v[80:81], v[18:19], v[18:19]
	v_pk_fma_f32 v[78:79], v[58:59], v[58:59], v[78:79]
	v_pk_fma_f32 v[76:77], v[60:61], v[60:61], v[76:77]
	v_pk_fma_f32 v[74:75], v[52:53], v[52:53], v[74:75]
	v_pk_fma_f32 v[72:73], v[64:65], v[64:65], v[72:73]
	v_pk_fma_f32 v[70:71], v[56:57], v[56:57], v[70:71]
	v_pk_fma_f32 v[68:69], v[62:63], v[62:63], v[68:69]
	v_pk_fma_f32 v[66:67], v[54:55], v[54:55], v[66:67]
	v_pk_fma_f32 v[80:81], v[50:51], v[50:51], v[80:81]
	v_pk_add_f32 v[66:67], v[66:67], v[68:69]
	v_pk_add_f32 v[68:69], v[70:71], v[72:73]
	v_pk_add_f32 v[70:71], v[74:75], v[76:77]
	v_pk_add_f32 v[72:73], v[80:81], v[78:79]
	v_pk_add_f32 v[68:69], v[70:71], v[68:69]
	v_pk_add_f32 v[66:67], v[72:73], v[66:67]
	v_pk_mul_f32 v[72:73], v[14:15], v[14:15]
	v_pk_mov_b32 v[70:71], v[66:67], v[68:69] op_sel:[1,0]
	v_mov_b32_e32 v67, v69
	v_pk_add_f32 v[66:67], v[70:71], v[66:67]
	v_pk_mul_f32 v[70:71], v[6:7], v[6:7]
	v_pk_mul_f32 v[74:75], v[8:9], v[8:9]
	v_pk_mul_f32 v[76:77], v[16:17], v[16:17]
	v_pk_mul_f32 v[78:79], v[4:5], v[4:5]
	v_pk_mul_f32 v[80:81], v[12:13], v[12:13]
	v_pk_mul_f32 v[82:83], v[10:11], v[10:11]
	v_pk_mul_f32 v[84:85], v[2:3], v[2:3]
	v_pk_fma_f32 v[82:83], v[42:43], v[42:43], v[82:83]
	v_pk_fma_f32 v[80:81], v[44:45], v[44:45], v[80:81]
	v_pk_fma_f32 v[78:79], v[36:37], v[36:37], v[78:79]
	v_pk_fma_f32 v[76:77], v[48:49], v[48:49], v[76:77]
	v_pk_fma_f32 v[74:75], v[40:41], v[40:41], v[74:75]
	v_pk_fma_f32 v[72:73], v[46:47], v[46:47], v[72:73]
	v_pk_fma_f32 v[70:71], v[38:39], v[38:39], v[70:71]
	v_pk_fma_f32 v[84:85], v[34:35], v[34:35], v[84:85]
	v_pk_add_f32 v[70:71], v[70:71], v[72:73]
	v_pk_add_f32 v[72:73], v[74:75], v[76:77]
	v_pk_add_f32 v[74:75], v[78:79], v[80:81]
	v_pk_add_f32 v[76:77], v[84:85], v[82:83]
	v_pk_add_f32 v[72:73], v[74:75], v[72:73]
	v_pk_add_f32 v[70:71], v[76:77], v[70:71]
	v_pk_add_f32 v[66:67], v[66:67], v[66:67] op_sel:[0,1] op_sel_hi:[1,0]
	v_pk_mov_b32 v[74:75], v[70:71], v[72:73] op_sel:[1,0]
	v_mov_b32_e32 v71, v73
	v_pk_add_f32 v[70:71], v[74:75], v[70:71]
	v_mov_b32_e32 v69, v66
	v_pk_add_f32 v[70:71], v[70:71], v[70:71] op_sel:[0,1] op_sel_hi:[1,0]
	s_nop 0
	v_permlane32_swap_b32_e32 v66, v69
	v_mov_b32_e32 v68, v70
	s_nop 1
	v_permlane32_swap_b32_e32 v70, v68
	v_mov_b32_e32 v71, v66
	v_pk_add_f32 v[66:67], v[70:71], v[68:69]
	v_pk_fma_f32 v[66:67], v[66:67], s[0:1], v[152:153] op_sel_hi:[1,0,0]
	s_mov_b32 s1, 0x800000
	v_mul_f32_e32 v68, 0x4b800000, v67
	v_cmp_gt_f32_e32 vcc, s1, v67
	s_nop 1
	v_cndmask_b32_e32 v67, v67, v68, vcc
	v_rsq_f32_e32 v67, v67
	s_nop 0
	v_mul_f32_e32 v68, 0x45800000, v67
	v_cndmask_b32_e32 v68, v67, v68, vcc
	v_pk_mul_f32 v[158:159], v[50:51], v[68:69] op_sel_hi:[1,0]
	v_pk_mul_f32 v[50:51], v[18:19], v[68:69] op_sel_hi:[1,0]
	v_mul_f32_e32 v18, 0x4b800000, v66
	v_cmp_gt_f32_e32 vcc, s1, v66
	v_pk_mul_f32 v[80:81], v[60:61], v[68:69] op_sel_hi:[1,0]
	v_pk_mul_f32 v[60:61], v[28:29], v[68:69] op_sel_hi:[1,0]
	v_cndmask_b32_e32 v18, v66, v18, vcc
	v_rsq_f32_e32 v18, v18
	v_pk_mul_f32 v[78:79], v[58:59], v[68:69] op_sel_hi:[1,0]
	v_pk_mul_f32 v[160:161], v[52:53], v[68:69] op_sel_hi:[1,0]
	v_pk_mul_f32 v[82:83], v[54:55], v[68:69] op_sel_hi:[1,0]
	v_mul_f32_e32 v19, 0x45800000, v18
	v_cndmask_b32_e32 v28, v18, v19, vcc
	v_pk_mul_f32 v[168:169], v[56:57], v[68:69] op_sel_hi:[1,0]
	v_pk_mul_f32 v[58:59], v[26:27], v[68:69] op_sel_hi:[1,0]
	v_pk_mul_f32 v[52:53], v[20:21], v[68:69] op_sel_hi:[1,0]
	v_pk_mul_f32 v[54:55], v[22:23], v[68:69] op_sel_hi:[1,0]
	v_pk_mul_f32 v[56:57], v[24:25], v[68:69] op_sel_hi:[1,0]
	v_pk_mul_f32 v[18:19], v[42:43], v[28:29] op_sel_hi:[1,0]
	v_pk_mul_f32 v[20:21], v[44:45], v[28:29] op_sel_hi:[1,0]
	v_pk_mul_f32 v[22:23], v[46:47], v[28:29] op_sel_hi:[1,0]
	v_pk_mul_f32 v[26:27], v[48:49], v[28:29] op_sel_hi:[1,0]
	v_pk_mul_f32 v[162:163], v[34:35], v[28:29] op_sel_hi:[1,0]
	v_pk_mul_f32 v[164:165], v[36:37], v[28:29] op_sel_hi:[1,0]
	v_pk_mul_f32 v[166:167], v[38:39], v[28:29] op_sel_hi:[1,0]
	v_pk_mul_f32 v[24:25], v[40:41], v[28:29] op_sel_hi:[1,0]
	v_pk_mul_f32 v[104:105], v[2:3], v[28:29] op_sel_hi:[1,0]
	v_pk_mul_f32 v[112:113], v[4:5], v[28:29] op_sel_hi:[1,0]
	s_nop 0
	s_nop 0
	ds_read_b128 v[2:5], v150 offset:60416
	ds_read_b128 v[34:37], v174 offset:32768
	ds_read_b128 v[38:41], v174 offset:32800
	ds_read_b128 v[42:45], v174 offset:32832
	ds_read_b128 v[46:49], v174 offset:32864
	v_cvt_pk_bf16_f32 v129, v168, v169
	v_cvt_pk_bf16_f32 v128, v82, v83
	v_cvt_pk_bf16_f32 v127, v160, v161
	v_cvt_pk_bf16_f32 v126, v158, v159
	v_cvt_pk_bf16_f32 v137, v24, v25
	v_cvt_pk_bf16_f32 v136, v166, v167
	v_cvt_pk_bf16_f32 v135, v164, v165
	s_waitcnt lgkmcnt(0)
	v_mfma_f32_32x32x16_bf16 v[86:101], v[2:5], v[126:129], v[34:49]
	v_cvt_pk_bf16_f32 v134, v162, v163
	v_mul_f32_e32 v84, v62, v68
	v_mul_f32_e32 v85, v63, v68
	v_mul_f32_e32 v170, v64, v68
	v_mul_f32_e32 v171, v65, v68
	v_pk_mul_f32 v[62:63], v[30:31], v[68:69] op_sel_hi:[1,0]
	v_pk_mul_f32 v[64:65], v[32:33], v[68:69] op_sel_hi:[1,0]
	v_pk_mul_f32 v[116:117], v[6:7], v[28:29] op_sel_hi:[1,0]
	v_pk_mul_f32 v[154:155], v[8:9], v[28:29] op_sel_hi:[1,0]
	v_mfma_f32_32x32x16_bf16 v[34:49], v[2:5], v[134:137], v[34:49]
	ds_read_b128 v[6:9], v150 offset:61440
	ds_read_b128 v[66:69], v174 offset:32896
	ds_read_b128 v[106:109], v150 offset:64512
	v_cvt_pk_bf16_f32 v125, v170, v171
	v_cvt_pk_bf16_f32 v124, v84, v85
	v_cvt_pk_bf16_f32 v123, v80, v81
	v_cvt_pk_bf16_f32 v122, v78, v79
	v_cvt_pk_bf16_f32 v149, v26, v27
	v_cvt_pk_bf16_f32 v148, v22, v23
	v_cvt_pk_bf16_f32 v147, v20, v21
	v_cvt_pk_bf16_f32 v146, v18, v19
	s_waitcnt lgkmcnt(2)
	v_mfma_f32_32x32x16_bf16 v[86:101], v[6:9], v[122:125], v[86:101]
	v_mul_f32_e32 v102, v10, v28
	v_mul_f32_e32 v103, v11, v28
	v_mul_f32_e32 v110, v12, v28
	v_mul_f32_e32 v111, v13, v28
	v_mul_f32_e32 v114, v14, v28
	v_mul_f32_e32 v115, v15, v28
	v_pk_mul_f32 v[156:157], v[16:17], v[28:29] op_sel_hi:[1,0]
	ds_read_b128 v[176:179], v174 offset:33536
	ds_read_b128 v[180:183], v174 offset:33568
	ds_read_b128 v[184:187], v174 offset:33600
	ds_read_b128 v[28:31], v174 offset:33632
	ds_read_b128 v[188:191], v174 offset:33792
	ds_read_b128 v[192:195], v174 offset:33824
	ds_read_b128 v[196:199], v174 offset:33856
	ds_read_b128 v[200:203], v174 offset:33888
	ds_read_b128 v[204:207], v150 offset:62464
	v_cvt_pk_bf16_f32 v133, v56, v57
	v_mfma_f32_32x32x16_bf16 v[34:49], v[6:9], v[146:149], v[34:49]
	v_cvt_pk_bf16_f32 v132, v54, v55
	v_cvt_pk_bf16_f32 v131, v52, v53
	v_cvt_pk_bf16_f32 v130, v50, v51
	ds_read_b128 v[70:73], v174 offset:33664
	ds_read_b128 v[74:77], v174 offset:33920
	ds_read_b128 v[208:211], v150 offset:63488
	v_cvt_pk_bf16_f32 v145, v154, v155
	v_cvt_pk_bf16_f32 v144, v116, v117
	v_cvt_pk_bf16_f32 v143, v112, v113
	v_cvt_pk_bf16_f32 v142, v104, v105
	s_waitcnt lgkmcnt(3)
	v_mfma_f32_32x32x16_bf16 v[86:101], v[204:207], v[130:133], v[86:101]
	v_cvt_pk_bf16_f32 v121, v64, v65
	v_cvt_pk_bf16_f32 v120, v62, v63
	v_cvt_pk_bf16_f32 v119, v60, v61
	v_cvt_pk_bf16_f32 v118, v58, v59
	v_cvt_pk_bf16_f32 v141, v156, v157
	v_cvt_pk_bf16_f32 v140, v114, v115
	v_cvt_pk_bf16_f32 v139, v110, v111
	v_mfma_f32_32x32x16_bf16 v[34:49], v[204:207], v[142:145], v[34:49]
	v_cvt_pk_bf16_f32 v138, v102, v103
	v_fma_f32 v16, v30, v170, v202
	v_fma_f32 v17, v31, v171, v203
	v_fma_f32 v14, v28, v84, v200
	v_fma_f32 v15, v29, v85, v201
	v_pk_fma_f32 v[12:13], v[186:187], v[80:81], v[198:199]
	v_pk_fma_f32 v[10:11], v[184:185], v[78:79], v[196:197]
	v_pk_fma_f32 v[8:9], v[182:183], v[168:169], v[194:195]
	s_waitcnt lgkmcnt(0)
	v_mfma_f32_32x32x16_bf16 v[86:101], v[208:211], v[118:121], v[86:101]
	v_fma_f32 v6, v180, v82, v192
	v_fma_f32 v7, v181, v83, v193
	ds_read_b128 v[78:81], v174 offset:33760
	ds_read_b128 v[82:85], v174 offset:33248
	v_fma_f32 v4, v178, v160, v190
	v_fma_f32 v5, v179, v161, v191
	v_pk_fma_f32 v[2:3], v[176:177], v[158:159], v[188:189]
	v_pk_fma_f32 v[32:33], v[30:31], v[26:27], v[202:203]
	v_pk_fma_f32 v[30:31], v[28:29], v[22:23], v[200:201]
	v_pk_fma_f32 v[28:29], v[186:187], v[20:21], v[198:199]
	v_pk_fma_f32 v[26:27], v[184:185], v[18:19], v[196:197]
	v_pk_fma_f32 v[24:25], v[182:183], v[24:25], v[194:195]
	v_pk_fma_f32 v[22:23], v[180:181], v[166:167], v[192:193]
	v_pk_fma_f32 v[20:21], v[178:179], v[164:165], v[190:191]
	v_pk_fma_f32 v[18:19], v[176:177], v[162:163], v[188:189]
	ds_read_b128 v[158:161], v174 offset:33696
	ds_read_b128 v[162:165], v174 offset:33728
	ds_read_b128 v[166:169], v174 offset:33952
	ds_read_b128 v[176:179], v174 offset:33984
	ds_read_b128 v[180:183], v174 offset:34016
	ds_read_b128 v[184:187], v212 offset:11264
	v_mfma_f32_32x32x16_bf16 v[34:49], v[208:211], v[138:141], v[34:49]
	v_cvt_pk_bf16_f32 v86, v86, v87
	v_cvt_pk_bf16_f32 v87, v88, v89
	v_cvt_pk_bf16_f32 v88, v90, v91
	v_cvt_pk_bf16_f32 v89, v92, v93
	ds_read_b128 v[90:93], v212 offset:12288
	v_pk_max_i16 v86, v86, 0
	v_pk_max_i16 v87, v87, 0
	v_pk_max_i16 v88, v88, 0
	v_pk_max_i16 v89, v89, 0
	s_nop 1
	s_nop 0
	v_cvt_pk_bf16_f32 v188, v34, v35
	v_cvt_pk_bf16_f32 v189, v36, v37
	v_cvt_pk_bf16_f32 v190, v38, v39
	v_cvt_pk_bf16_f32 v191, v40, v41
	s_waitcnt lgkmcnt(1)
	v_mfma_f32_32x32x16_bf16 v[2:17], v[184:187], v[86:89], v[2:17]
	v_pk_max_i16 v188, v188, 0
	v_pk_max_i16 v189, v189, 0
	v_pk_max_i16 v190, v190, 0
	v_pk_max_i16 v191, v191, 0
	v_cvt_pk_bf16_f32 v94, v94, v95
	v_cvt_pk_bf16_f32 v95, v96, v97
	v_cvt_pk_bf16_f32 v96, v98, v99
	v_cvt_pk_bf16_f32 v97, v100, v101
	v_cvt_pk_bf16_f32 v98, v42, v43
	v_cvt_pk_bf16_f32 v99, v44, v45
	v_mfma_f32_32x32x16_bf16 v[18:33], v[184:187], v[188:191], v[18:33]
	ds_read_b128 v[184:187], v212 offset:19456
	v_cvt_pk_bf16_f32 v100, v46, v47
	v_cvt_pk_bf16_f32 v101, v48, v49
	v_fma_f32 v64, v80, v64, v182
	v_fma_f32 v65, v81, v65, v183
	v_pk_fma_f32 v[62:63], v[78:79], v[62:63], v[180:181]
	v_pk_fma_f32 v[60:61], v[164:165], v[60:61], v[178:179]
	v_pk_fma_f32 v[58:59], v[162:163], v[58:59], v[176:177]
	v_pk_max_i16 v94, v94, 0
	v_pk_max_i16 v95, v95, 0
	v_pk_max_i16 v96, v96, 0
	v_pk_max_i16 v97, v97, 0
	v_pk_max_i16 v98, v98, 0
	v_pk_max_i16 v99, v99, 0
	v_pk_max_i16 v100, v100, 0
	v_pk_max_i16 v101, v101, 0
	v_pk_fma_f32 v[56:57], v[160:161], v[56:57], v[168:169]
	s_waitcnt lgkmcnt(1)
	v_mfma_f32_32x32x16_bf16 v[2:17], v[90:93], v[94:97], v[2:17]
	v_fma_f32 v54, v158, v54, v166
	v_fma_f32 v55, v159, v55, v167
	v_fma_f32 v52, v72, v52, v76
	v_fma_f32 v53, v73, v53, v77
	v_fma_f32 v50, v70, v50, v74
	v_fma_f32 v51, v71, v51, v75
	v_pk_fma_f32 v[48:49], v[80:81], v[156:157], v[182:183]
	v_pk_fma_f32 v[46:47], v[78:79], v[114:115], v[180:181]
	v_pk_fma_f32 v[44:45], v[164:165], v[110:111], v[178:179]
	v_pk_fma_f32 v[42:43], v[162:163], v[102:103], v[176:177]
	v_mfma_f32_32x32x16_bf16 v[18:33], v[90:93], v[98:101], v[18:33]
	ds_read_b128 v[90:93], v212 offset:20480
	v_fma_f32 v40, v160, v154, v168
	v_fma_f32 v41, v161, v155, v169
	v_fma_f32 v38, v158, v116, v166
	v_fma_f32 v39, v159, v117, v167
	v_pk_fma_f32 v[36:37], v[72:73], v[112:113], v[76:77]
	v_pk_fma_f32 v[34:35], v[70:71], v[104:105], v[74:75]
	s_waitcnt lgkmcnt(1)
	v_mfma_f32_32x32x16_bf16 v[50:65], v[184:187], v[86:89], v[50:65]
	ds_read_b128 v[70:73], v174 offset:32928
	ds_read_b128 v[74:77], v174 offset:32960
	ds_read_b128 v[78:81], v174 offset:32992
	ds_read_b128 v[86:89], v174 offset:33024
	ds_read_b128 v[110:113], v212 offset:1024
	v_mfma_f32_32x32x16_bf16 v[34:49], v[184:187], v[188:191], v[34:49]
	s_waitcnt lgkmcnt(5)
	v_mfma_f32_32x32x16_bf16 v[50:65], v[90:93], v[94:97], v[50:65]
	v_mfma_f32_32x32x16_bf16 v[34:49], v[90:93], v[98:101], v[34:49]
	s_waitcnt lgkmcnt(2)
	v_mfma_f32_32x32x16_bf16 v[90:105], v[106:109], v[126:129], v[66:81]
	v_mfma_f32_32x32x16_bf16 v[66:81], v[106:109], v[134:137], v[66:81]
	ds_read_b128 v[106:109], v212 offset:0
	s_waitcnt lgkmcnt(0)
	v_mfma_f32_32x32x16_bf16 v[90:105], v[106:109], v[122:125], v[90:105]
	v_mfma_f32_32x32x16_bf16 v[66:81], v[106:109], v[146:149], v[66:81]
	ds_read_b128 v[106:109], v212 offset:2048
	v_mfma_f32_32x32x16_bf16 v[90:105], v[110:113], v[130:133], v[90:105]
	v_mfma_f32_32x32x16_bf16 v[66:81], v[110:113], v[142:145], v[66:81]
	ds_read_b128 v[110:113], v212 offset:13312
	s_waitcnt lgkmcnt(1)
	v_mfma_f32_32x32x16_bf16 v[90:105], v[106:109], v[118:121], v[90:105]
	v_mfma_f32_32x32x16_bf16 v[66:81], v[106:109], v[138:141], v[66:81]
	s_nop 10
	v_cvt_pk_bf16_f32 v90, v90, v91
	v_cvt_pk_bf16_f32 v91, v92, v93
	v_cvt_pk_bf16_f32 v92, v94, v95
	v_cvt_pk_bf16_f32 v94, v98, v99
	v_cvt_pk_bf16_f32 v95, v100, v101
	ds_read_b128 v[98:101], v212 offset:21504
	v_cvt_pk_bf16_f32 v66, v66, v67
	v_cvt_pk_bf16_f32 v67, v68, v69
	v_cvt_pk_bf16_f32 v68, v70, v71
	v_cvt_pk_bf16_f32 v93, v96, v97
	v_cvt_pk_bf16_f32 v69, v72, v73
	ds_read_b128 v[70:73], v212 offset:14336
	v_pk_max_i16 v90, v90, 0
	v_pk_max_i16 v91, v91, 0
	v_pk_max_i16 v92, v92, 0
	v_pk_max_i16 v93, v93, 0
	v_pk_max_i16 v66, v66, 0
	v_pk_max_i16 v67, v67, 0
	v_pk_max_i16 v68, v68, 0
	v_pk_max_i16 v69, v69, 0
	v_cvt_pk_bf16_f32 v96, v102, v103
	s_waitcnt lgkmcnt(2)
	v_mfma_f32_32x32x16_bf16 v[2:17], v[110:113], v[90:93], v[2:17]
	v_cvt_pk_bf16_f32 v97, v104, v105
	v_cvt_pk_bf16_f32 v74, v74, v75
	v_cvt_pk_bf16_f32 v75, v76, v77
	v_cvt_pk_bf16_f32 v76, v78, v79
	v_cvt_pk_bf16_f32 v77, v80, v81
	v_pk_max_i16 v94, v94, 0
	v_pk_max_i16 v95, v95, 0
	v_pk_max_i16 v96, v96, 0
	v_pk_max_i16 v97, v97, 0
	v_pk_max_i16 v74, v74, 0
	v_pk_max_i16 v75, v75, 0
	v_pk_max_i16 v76, v76, 0
	v_pk_max_i16 v77, v77, 0
	v_mfma_f32_32x32x16_bf16 v[18:33], v[110:113], v[66:69], v[18:33]
	s_waitcnt lgkmcnt(1)
	v_mfma_f32_32x32x16_bf16 v[34:49], v[98:101], v[66:69], v[34:49]
	ds_read_b128 v[66:69], v212 offset:22528
	v_mfma_f32_32x32x16_bf16 v[50:65], v[98:101], v[90:93], v[50:65]
	s_waitcnt lgkmcnt(1)
	v_mfma_f32_32x32x16_bf16 v[2:17], v[70:73], v[94:97], v[2:17]
	v_mfma_f32_32x32x16_bf16 v[18:33], v[70:73], v[74:77], v[18:33]
	ds_read_b128 v[78:81], v212 offset:3072
	s_waitcnt lgkmcnt(1)
	v_mfma_f32_32x32x16_bf16 v[50:65], v[66:69], v[94:97], v[50:65]
	ds_read_b128 v[90:93], v174 offset:33056
	ds_read_b128 v[94:97], v174 offset:33088
	ds_read_b128 v[98:101], v174 offset:33120
	ds_read_b128 v[70:73], v174 offset:33152
	v_mfma_f32_32x32x16_bf16 v[34:49], v[66:69], v[74:77], v[34:49]
	ds_read_b128 v[66:69], v212 offset:4096
	ds_read_b128 v[74:77], v212 offset:5120
	s_waitcnt lgkmcnt(3)
	v_mfma_f32_32x32x16_bf16 v[102:117], v[78:81], v[126:129], v[86:101]
	v_mfma_f32_32x32x16_bf16 v[86:101], v[78:81], v[134:137], v[86:101]
	s_waitcnt lgkmcnt(1)
	v_mfma_f32_32x32x16_bf16 v[86:101], v[66:69], v[146:149], v[86:101]
	v_mfma_f32_32x32x16_bf16 v[102:117], v[66:69], v[122:125], v[102:117]
	ds_read_b128 v[66:69], v212 offset:6144
	s_waitcnt lgkmcnt(1)
	v_mfma_f32_32x32x16_bf16 v[86:101], v[74:77], v[142:145], v[86:101]
	v_mfma_f32_32x32x16_bf16 v[102:117], v[74:77], v[130:133], v[102:117]
	ds_read_b128 v[74:77], v212 offset:15360
	s_waitcnt lgkmcnt(1)
	v_mfma_f32_32x32x16_bf16 v[86:101], v[66:69], v[138:141], v[86:101]
	v_mfma_f32_32x32x16_bf16 v[102:117], v[66:69], v[118:121], v[102:117]
	s_nop 10
	v_cvt_pk_bf16_f32 v78, v86, v87
	v_cvt_pk_bf16_f32 v80, v90, v91
	v_cvt_pk_bf16_f32 v79, v88, v89
	v_cvt_pk_bf16_f32 v81, v92, v93
	ds_read_b128 v[86:89], v212 offset:16384
	ds_read_b128 v[90:93], v212 offset:23552
	v_cvt_pk_bf16_f32 v66, v102, v103
	v_cvt_pk_bf16_f32 v67, v104, v105
	v_cvt_pk_bf16_f32 v68, v106, v107
	v_cvt_pk_bf16_f32 v69, v108, v109
	v_pk_max_i16 v66, v66, 0
	v_pk_max_i16 v67, v67, 0
	v_pk_max_i16 v68, v68, 0
	v_pk_max_i16 v69, v69, 0
	v_pk_max_i16 v78, v78, 0
	v_pk_max_i16 v79, v79, 0
	v_pk_max_i16 v80, v80, 0
	v_pk_max_i16 v81, v81, 0
	v_cvt_pk_bf16_f32 v94, v94, v95
	s_waitcnt lgkmcnt(2)
	v_mfma_f32_32x32x16_bf16 v[18:33], v[74:77], v[78:81], v[18:33]
	v_cvt_pk_bf16_f32 v95, v96, v97
	v_cvt_pk_bf16_f32 v96, v98, v99
	v_cvt_pk_bf16_f32 v97, v100, v101
	v_pk_max_i16 v94, v94, 0
	v_pk_max_i16 v95, v95, 0
	v_pk_max_i16 v96, v96, 0
	v_pk_max_i16 v97, v97, 0
	v_mfma_f32_32x32x16_bf16 v[2:17], v[74:77], v[66:69], v[2:17]
	v_cvt_pk_bf16_f32 v74, v110, v111
	v_cvt_pk_bf16_f32 v75, v112, v113
	v_cvt_pk_bf16_f32 v76, v114, v115
	v_cvt_pk_bf16_f32 v77, v116, v117
	v_pk_max_i16 v74, v74, 0
	v_pk_max_i16 v75, v75, 0
	v_pk_max_i16 v76, v76, 0
	v_pk_max_i16 v77, v77, 0
	s_waitcnt lgkmcnt(0)
	v_mfma_f32_32x32x16_bf16 v[50:65], v[90:93], v[66:69], v[50:65]
	ds_read_b128 v[66:69], v212 offset:24576
	v_mfma_f32_32x32x16_bf16 v[34:49], v[90:93], v[78:81], v[34:49]
	ds_read_b128 v[102:105], v212 offset:7168
	v_mfma_f32_32x32x16_bf16 v[2:17], v[86:89], v[74:77], v[2:17]
	s_waitcnt lgkmcnt(1)
	v_mfma_f32_32x32x16_bf16 v[50:65], v[66:69], v[74:77], v[50:65]
	ds_read_b128 v[74:77], v174 offset:33184
	ds_read_b128 v[78:81], v174 offset:33216
	v_mfma_f32_32x32x16_bf16 v[34:49], v[66:69], v[94:97], v[34:49]
	ds_read_b128 v[66:69], v212 offset:8192
	v_mfma_f32_32x32x16_bf16 v[18:33], v[86:89], v[94:97], v[18:33]
	s_waitcnt lgkmcnt(1)
	v_mfma_f32_32x32x16_bf16 v[86:101], v[102:105], v[126:129], v[70:85]
	v_mfma_f32_32x32x16_bf16 v[70:85], v[102:105], v[134:137], v[70:85]
	ds_read_b128 v[102:105], v212 offset:9216
	v_lshlrev_b32_e32 v135, 2, v1
	v_add_u32_e32 v134, v172, v174
	s_waitcnt lgkmcnt(1)
	v_mfma_f32_32x32x16_bf16 v[86:101], v[66:69], v[122:125], v[86:101]
	v_mfma_f32_32x32x16_bf16 v[70:85], v[66:69], v[146:149], v[70:85]
	ds_read_b128 v[66:69], v212 offset:10240
	s_waitcnt lgkmcnt(1)
	v_mfma_f32_32x32x16_bf16 v[86:101], v[102:105], v[130:133], v[86:101]
	v_mfma_f32_32x32x16_bf16 v[70:85], v[102:105], v[142:145], v[70:85]
	ds_read_b128 v[102:105], v212 offset:17408
	s_waitcnt lgkmcnt(1)
	v_mfma_f32_32x32x16_bf16 v[86:101], v[66:69], v[118:121], v[86:101]
	v_mfma_f32_32x32x16_bf16 v[70:85], v[66:69], v[138:141], v[70:85]
	s_nop 10
	v_cvt_pk_bf16_f32 v68, v90, v91
	v_cvt_pk_bf16_f32 v69, v92, v93
	ds_read_b128 v[90:93], v212 offset:25600
	v_cvt_pk_bf16_f32 v66, v86, v87
	v_cvt_pk_bf16_f32 v67, v88, v89
	v_pk_max_i16 v66, v66, 0
	v_pk_max_i16 v67, v67, 0
	v_pk_max_i16 v68, v68, 0
	v_pk_max_i16 v69, v69, 0
	v_cvt_pk_bf16_f32 v70, v70, v71
	v_cvt_pk_bf16_f32 v71, v72, v73
	s_waitcnt lgkmcnt(1)
	v_mfma_f32_32x32x16_bf16 v[2:17], v[102:105], v[66:69], v[2:17]
	v_cvt_pk_bf16_f32 v72, v74, v75
	v_cvt_pk_bf16_f32 v73, v76, v77
	ds_read_b128 v[74:77], v212 offset:18432
	v_cvt_pk_bf16_f32 v86, v94, v95
	v_cvt_pk_bf16_f32 v87, v96, v97
	v_cvt_pk_bf16_f32 v88, v98, v99
	s_waitcnt lgkmcnt(1)
	v_mfma_f32_32x32x16_bf16 v[50:65], v[90:93], v[66:69], v[50:65]
	ds_read_b128 v[66:69], v212 offset:26624
	v_cvt_pk_bf16_f32 v89, v100, v101
	v_pk_max_i16 v86, v86, 0
	v_pk_max_i16 v87, v87, 0
	v_pk_max_i16 v88, v88, 0
	v_pk_max_i16 v89, v89, 0
	v_pk_max_i16 v70, v70, 0
	v_pk_max_i16 v71, v71, 0
	v_pk_max_i16 v72, v72, 0
	v_pk_max_i16 v73, v73, 0
	v_cvt_pk_bf16_f32 v78, v78, v79
	v_cvt_pk_bf16_f32 v79, v80, v81
	s_waitcnt lgkmcnt(1)
	v_mfma_f32_32x32x16_bf16 v[2:17], v[74:77], v[86:89], v[2:17]
	v_cvt_pk_bf16_f32 v80, v82, v83
	v_cvt_pk_bf16_f32 v81, v84, v85
	v_pk_max_i16 v78, v78, 0
	v_pk_max_i16 v79, v79, 0
	v_pk_max_i16 v80, v80, 0
	v_pk_max_i16 v81, v81, 0
	s_waitcnt lgkmcnt(0)
	v_mfma_f32_32x32x16_bf16 v[50:65], v[66:69], v[86:89], v[50:65]
	v_mfma_f32_32x32x16_bf16 v[34:49], v[90:93], v[70:73], v[34:49]
	s_nop 10
	v_add_f32_e32 v130, v10, v58
	v_add_f32_e32 v131, v11, v59
	v_add_f32_e32 v132, v12, v60
	v_add_f32_e32 v133, v13, v61
	v_add_f32_e32 v138, v4, v52
	v_add_f32_e32 v139, v5, v53
	v_pk_add_f32 v[140:141], v[16:17], v[64:65]
	v_pk_add_f32 v[142:143], v[8:9], v[56:57]
	v_pk_add_f32 v[144:145], v[14:15], v[62:63]
	v_pk_add_f32 v[146:147], v[6:7], v[54:55]
	v_mfma_f32_32x32x16_bf16 v[18:33], v[102:105], v[70:73], v[18:33]
	ds_read2st64_b32 v[70:71], v135 offset0:133 offset1:134
	v_add_f32_e32 v148, v2, v50
	v_add_f32_e32 v149, v3, v51
	v_add_f32_e32 v144, v146, v144
	v_add_f32_e32 v145, v147, v145
	v_pk_add_f32 v[140:141], v[142:143], v[140:141]
	v_pk_add_f32 v[132:133], v[138:139], v[132:133]
	v_pk_add_f32 v[130:131], v[148:149], v[130:131]
	v_pk_add_f32 v[132:133], v[132:133], v[140:141]
	v_pk_add_f32 v[130:131], v[130:131], v[144:145]
	v_mfma_f32_32x32x16_bf16 v[34:49], v[66:69], v[78:81], v[34:49]
	v_pk_mov_b32 v[138:139], v[130:131], v[132:133] op_sel:[1,0]
	v_mov_b32_e32 v131, v133
	s_waitcnt vmcnt(0) lgkmcnt(0)
	v_mul_f32_e32 v66, v175, v70
	v_pk_add_f32 v[130:131], v[138:139], v[130:131]
	ds_write_b32 v173, v66 offset:512
	v_mul_f32_e32 v66, v175, v71
	v_pk_add_f32 v[130:131], v[130:131], v[130:131] op_sel:[0,1] op_sel_hi:[1,0]
	s_waitcnt lgkmcnt(0)
	ds_read_b128 v[102:105], v174 offset:34560
	ds_read_b128 v[98:101], v174 offset:34592
	ds_read_b128 v[110:113], v174 offset:34624
	ds_read_b128 v[106:109], v174 offset:34656
	ds_read_b128 v[114:117], v174 offset:34688
	ds_read_b128 v[122:125], v174 offset:34720
	ds_read_b128 v[118:121], v174 offset:34752
	ds_read_b128 v[126:129], v174 offset:34784
	v_mov_b32_dpp v66, v66 quad_perm:[1,0,3,2] row_mask:0xf bank_mask:0xf bound_ctrl:1
	v_mov_b32_e32 v131, v130
	v_fmac_f32_e32 v66, v175, v71
	s_nop 0
	v_permlane32_swap_b32_e32 v130, v131
	v_add_f32_dpp v66, v66, v66 quad_perm:[2,3,0,1] row_mask:0xf bank_mask:0xf bound_ctrl:1
	v_add_f32_e32 v130, v130, v131
	v_fmamk_f32 v65, v130, 0xbc800000, v65
	v_add_f32_dpp v66, v66, v66 row_half_mirror row_mask:0xf bank_mask:0xf bound_ctrl:1
	v_fmamk_f32 v64, v130, 0xbc800000, v64
	v_fmamk_f32 v63, v130, 0xbc800000, v63
	v_fmamk_f32 v62, v130, 0xbc800000, v62
	v_fmamk_f32 v61, v130, 0xbc800000, v61
	v_fmamk_f32 v60, v130, 0xbc800000, v60
	v_fmamk_f32 v59, v130, 0xbc800000, v59
	v_fmamk_f32 v58, v130, 0xbc800000, v58
	v_fmamk_f32 v57, v130, 0xbc800000, v57
	v_fmamk_f32 v56, v130, 0xbc800000, v56
	v_fmamk_f32 v55, v130, 0xbc800000, v55
	v_fmamk_f32 v54, v130, 0xbc800000, v54
	v_fmamk_f32 v53, v130, 0xbc800000, v53
	v_fmamk_f32 v52, v130, 0xbc800000, v52
	v_fmamk_f32 v51, v130, 0xbc800000, v51
	v_fmac_f32_e32 v50, 0xbc800000, v130
	v_add_f32_dpp v66, v66, v66 row_ror:8 row_mask:0xf bank_mask:0xf bound_ctrl:1
	v_fmamk_f32 v17, v130, 0xbc800000, v17
	v_fmamk_f32 v16, v130, 0xbc800000, v16
	v_fmamk_f32 v15, v130, 0xbc800000, v15
	v_fmamk_f32 v14, v130, 0xbc800000, v14
	v_fmamk_f32 v13, v130, 0xbc800000, v13
	v_fmamk_f32 v12, v130, 0xbc800000, v12
	v_fmamk_f32 v11, v130, 0xbc800000, v11
	v_fmamk_f32 v10, v130, 0xbc800000, v10
	v_fmamk_f32 v9, v130, 0xbc800000, v9
	v_fmamk_f32 v8, v130, 0xbc800000, v8
	v_fmamk_f32 v7, v130, 0xbc800000, v7
	v_fmamk_f32 v6, v130, 0xbc800000, v6
	v_fmamk_f32 v5, v130, 0xbc800000, v5
	v_fmamk_f32 v4, v130, 0xbc800000, v4
	v_fmamk_f32 v3, v130, 0xbc800000, v3
	v_fmac_f32_e32 v2, 0xbc800000, v130
	v_pk_mul_f32 v[130:131], v[54:55], v[54:55]
	v_pk_mul_f32 v[132:133], v[62:63], v[62:63]
	v_pk_mul_f32 v[138:139], v[50:51], v[50:51]
	v_pk_mul_f32 v[140:141], v[58:59], v[58:59]
	v_pk_mul_f32 v[142:143], v[56:57], v[56:57]
	v_pk_mul_f32 v[144:145], v[64:65], v[64:65]
	v_pk_mul_f32 v[146:147], v[52:53], v[52:53]
	v_pk_mul_f32 v[148:149], v[60:61], v[60:61]
	v_mov_b32_e32 v67, v66
	v_pk_fma_f32 v[148:149], v[12:13], v[12:13], v[148:149]
	v_pk_fma_f32 v[146:147], v[4:5], v[4:5], v[146:147]
	v_pk_fma_f32 v[144:145], v[16:17], v[16:17], v[144:145]
	v_pk_fma_f32 v[142:143], v[8:9], v[8:9], v[142:143]
	v_pk_fma_f32 v[140:141], v[10:11], v[10:11], v[140:141]
	v_pk_fma_f32 v[138:139], v[2:3], v[2:3], v[138:139]
	v_pk_fma_f32 v[132:133], v[14:15], v[14:15], v[132:133]
	v_pk_fma_f32 v[130:131], v[6:7], v[6:7], v[130:131]
	v_permlane16_swap_b32_e32 v66, v67
	v_pk_add_f32 v[130:131], v[130:131], v[132:133]
	v_pk_add_f32 v[132:133], v[138:139], v[140:141]
	v_pk_add_f32 v[138:139], v[142:143], v[144:145]
	v_pk_add_f32 v[140:141], v[146:147], v[148:149]
	v_mfma_f32_32x32x16_bf16 v[18:33], v[74:77], v[78:81], v[18:33]
	v_add_f32_e32 v136, v66, v67
	ds_read_b128 v[70:73], v134 offset:512
	ds_read_b128 v[66:69], v134 offset:544
	ds_read_b128 v[78:81], v134 offset:576
	ds_read_b128 v[74:77], v134 offset:608
	ds_read_b128 v[82:85], v134 offset:640
	ds_read_b128 v[90:93], v134 offset:672
	ds_read_b128 v[86:89], v134 offset:704
	ds_read_b128 v[94:97], v134 offset:736
	v_pk_add_f32 v[138:139], v[140:141], v[138:139]
	v_pk_add_f32 v[130:131], v[132:133], v[130:131]
	s_waitcnt lgkmcnt(8)
	v_pk_mul_f32 v[140:141], v[126:127], v[62:63]
	v_pk_mov_b32 v[132:133], v[130:131], v[138:139] op_sel:[1,0]
	v_mov_b32_e32 v131, v139
	v_pk_mul_f32 v[138:139], v[122:123], v[54:55]
	v_pk_mul_f32 v[142:143], v[114:115], v[50:51]
	v_pk_mul_f32 v[144:145], v[118:119], v[58:59]
	v_pk_mul_f32 v[146:147], v[124:125], v[56:57]
	v_pk_mul_f32 v[148:149], v[128:129], v[64:65]
	v_pk_mul_f32 v[154:155], v[116:117], v[52:53]
	v_pk_mul_f32 v[156:157], v[120:121], v[60:61]
	v_pk_fma_f32 v[154:155], v[104:105], v[4:5], v[154:155]
	v_pk_fma_f32 v[156:157], v[112:113], v[12:13], v[156:157]
	v_pk_fma_f32 v[148:149], v[108:109], v[16:17], v[148:149]
	v_pk_fma_f32 v[146:147], v[100:101], v[8:9], v[146:147]
	v_pk_fma_f32 v[144:145], v[110:111], v[10:11], v[144:145]
	v_pk_fma_f32 v[142:143], v[102:103], v[2:3], v[142:143]
	v_pk_fma_f32 v[140:141], v[106:107], v[14:15], v[140:141]
	v_pk_fma_f32 v[138:139], v[98:99], v[6:7], v[138:139]
	v_pk_add_f32 v[130:131], v[132:133], v[130:131]
	v_pk_add_f32 v[138:139], v[138:139], v[140:141]
	v_pk_add_f32 v[140:141], v[142:143], v[144:145]
	v_pk_add_f32 v[142:143], v[146:147], v[148:149]
	v_pk_add_f32 v[144:145], v[154:155], v[156:157]
	v_pk_add_f32 v[132:133], v[130:131], v[130:131] op_sel:[0,1] op_sel_hi:[1,0]
	v_pk_add_f32 v[142:143], v[144:145], v[142:143]
	v_pk_add_f32 v[138:139], v[140:141], v[138:139]
	v_add_f32_e32 v133, v142, v143
	v_add_f32_e32 v130, v138, v139
	s_waitcnt lgkmcnt(2)
	v_pk_mul_f32 v[138:139], v[90:91], v[54:55]
	s_waitcnt lgkmcnt(0)
	v_pk_mul_f32 v[140:141], v[94:95], v[62:63]
	v_pk_mul_f32 v[142:143], v[82:83], v[50:51]
	v_pk_mul_f32 v[144:145], v[86:87], v[58:59]
	v_pk_mul_f32 v[146:147], v[92:93], v[56:57]
	v_pk_mul_f32 v[148:149], v[96:97], v[64:65]
	v_pk_mul_f32 v[154:155], v[84:85], v[52:53]
	v_pk_mul_f32 v[156:157], v[88:89], v[60:61]
	v_add_f32_e32 v130, v130, v133
	v_pk_fma_f32 v[156:157], v[80:81], v[12:13], v[156:157]
	v_pk_fma_f32 v[154:155], v[72:73], v[4:5], v[154:155]
	v_pk_fma_f32 v[148:149], v[76:77], v[16:17], v[148:149]
	v_pk_fma_f32 v[146:147], v[68:69], v[8:9], v[146:147]
	v_pk_fma_f32 v[144:145], v[78:79], v[10:11], v[144:145]
	v_pk_fma_f32 v[142:143], v[70:71], v[2:3], v[142:143]
	v_pk_fma_f32 v[140:141], v[74:75], v[14:15], v[140:141]
	v_pk_fma_f32 v[138:139], v[66:67], v[6:7], v[138:139]
	v_mov_b32_e32 v133, v130
	v_pk_add_f32 v[138:139], v[138:139], v[140:141]
	v_pk_add_f32 v[140:141], v[142:143], v[144:145]
	v_pk_add_f32 v[142:143], v[146:147], v[148:149]
	v_pk_add_f32 v[144:145], v[154:155], v[156:157]
	v_permlane32_swap_b32_e32 v130, v133
	v_pk_add_f32 v[142:143], v[144:145], v[142:143]
	v_add_f32_e32 v160, v130, v133
	v_pk_add_f32 v[138:139], v[140:141], v[138:139]
	v_add_f32_e32 v133, v142, v143
	v_pk_add_f32 v[140:141], v[26:27], v[42:43]
	v_pk_add_f32 v[142:143], v[28:29], v[44:45]
	v_pk_add_f32 v[144:145], v[20:21], v[36:37]
	v_pk_add_f32 v[146:147], v[32:33], v[48:49]
	v_pk_add_f32 v[148:149], v[24:25], v[40:41]
	v_pk_add_f32 v[154:155], v[30:31], v[46:47]
	v_pk_add_f32 v[156:157], v[22:23], v[38:39]
	v_pk_add_f32 v[158:159], v[18:19], v[34:35]
	v_pk_add_f32 v[154:155], v[156:157], v[154:155]
	v_pk_add_f32 v[146:147], v[148:149], v[146:147]
	v_pk_add_f32 v[142:143], v[144:145], v[142:143]
	v_pk_add_f32 v[140:141], v[158:159], v[140:141]
	v_pk_add_f32 v[142:143], v[142:143], v[146:147]
	v_pk_add_f32 v[140:141], v[140:141], v[154:155]
	v_add_f32_e32 v130, v138, v139
	v_pk_mov_b32 v[144:145], v[140:141], v[142:143] op_sel:[1,0]
	v_mov_b32_e32 v141, v143
	v_pk_add_f32 v[140:141], v[144:145], v[140:141]
	v_add_f32_e32 v133, v130, v133
	v_pk_add_f32 v[140:141], v[140:141], v[140:141] op_sel:[0,1] op_sel_hi:[1,0]
	v_mov_b32_e32 v131, v132
	v_mov_b32_e32 v130, v140
	s_nop 1
	v_permlane32_swap_b32_e32 v140, v130
	v_add_f32_e32 v130, v140, v130
	v_fmamk_f32 v49, v130, 0xbc800000, v49
	v_fmamk_f32 v48, v130, 0xbc800000, v48
	v_fmamk_f32 v47, v130, 0xbc800000, v47
	v_fmamk_f32 v46, v130, 0xbc800000, v46
	v_fmamk_f32 v45, v130, 0xbc800000, v45
	v_fmamk_f32 v44, v130, 0xbc800000, v44
	v_fmamk_f32 v43, v130, 0xbc800000, v43
	v_fmamk_f32 v42, v130, 0xbc800000, v42
	v_fmamk_f32 v41, v130, 0xbc800000, v41
	v_fmamk_f32 v40, v130, 0xbc800000, v40
	v_fmamk_f32 v39, v130, 0xbc800000, v39
	v_fmamk_f32 v38, v130, 0xbc800000, v38
	v_fmamk_f32 v37, v130, 0xbc800000, v37
	v_fmamk_f32 v36, v130, 0xbc800000, v36
	v_fmamk_f32 v35, v130, 0xbc800000, v35
	v_fmac_f32_e32 v34, 0xbc800000, v130
	v_fmamk_f32 v33, v130, 0xbc800000, v33
	v_fmamk_f32 v32, v130, 0xbc800000, v32
	v_fmamk_f32 v31, v130, 0xbc800000, v31
	v_fmamk_f32 v30, v130, 0xbc800000, v30
	v_fmamk_f32 v29, v130, 0xbc800000, v29
	v_fmamk_f32 v28, v130, 0xbc800000, v28
	v_fmamk_f32 v27, v130, 0xbc800000, v27
	v_fmamk_f32 v26, v130, 0xbc800000, v26
	v_fmamk_f32 v25, v130, 0xbc800000, v25
	v_fmamk_f32 v24, v130, 0xbc800000, v24
	v_fmamk_f32 v23, v130, 0xbc800000, v23
	v_fmamk_f32 v22, v130, 0xbc800000, v22
	v_fmamk_f32 v21, v130, 0xbc800000, v21
	v_fmamk_f32 v20, v130, 0xbc800000, v20
	v_fmamk_f32 v19, v130, 0xbc800000, v19
	v_fmac_f32_e32 v18, 0xbc800000, v130
	v_pk_mul_f32 v[140:141], v[38:39], v[38:39]
	v_pk_mul_f32 v[142:143], v[46:47], v[46:47]
	v_pk_mul_f32 v[144:145], v[34:35], v[34:35]
	v_pk_mul_f32 v[146:147], v[42:43], v[42:43]
	v_pk_mul_f32 v[148:149], v[40:41], v[40:41]
	v_pk_mul_f32 v[154:155], v[48:49], v[48:49]
	v_pk_mul_f32 v[156:157], v[36:37], v[36:37]
	v_pk_mul_f32 v[158:159], v[44:45], v[44:45]
	v_pk_fma_f32 v[156:157], v[20:21], v[20:21], v[156:157]
	v_pk_fma_f32 v[158:159], v[28:29], v[28:29], v[158:159]
	v_pk_fma_f32 v[154:155], v[32:33], v[32:33], v[154:155]
	v_pk_fma_f32 v[148:149], v[24:25], v[24:25], v[148:149]
	v_pk_fma_f32 v[146:147], v[26:27], v[26:27], v[146:147]
	v_pk_fma_f32 v[144:145], v[18:19], v[18:19], v[144:145]
	v_pk_fma_f32 v[142:143], v[30:31], v[30:31], v[142:143]
	v_pk_fma_f32 v[140:141], v[22:23], v[22:23], v[140:141]
	v_permlane32_swap_b32_e32 v132, v131
	v_pk_add_f32 v[140:141], v[140:141], v[142:143]
	v_pk_add_f32 v[142:143], v[144:145], v[146:147]
	v_pk_add_f32 v[144:145], v[148:149], v[154:155]
	v_pk_add_f32 v[146:147], v[156:157], v[158:159]
	v_pk_add_f32 v[140:141], v[142:143], v[140:141]
	v_pk_add_f32 v[144:145], v[146:147], v[144:145]
	v_pk_mul_f32 v[122:123], v[122:123], v[38:39]
	v_pk_mov_b32 v[142:143], v[140:141], v[144:145] op_sel:[1,0]
	v_mov_b32_e32 v141, v145
	v_pk_add_f32 v[140:141], v[142:143], v[140:141]
	v_pk_mul_f32 v[126:127], v[126:127], v[46:47]
	v_pk_add_f32 v[140:141], v[140:141], v[140:141] op_sel:[0,1] op_sel_hi:[1,0]
	v_pk_mul_f32 v[114:115], v[114:115], v[34:35]
	v_mov_b32_e32 v130, v140
	s_nop 1
	v_permlane32_swap_b32_e32 v140, v130
	v_mov_b32_e32 v141, v132
	v_pk_add_f32 v[130:131], v[140:141], v[130:131]
	v_pk_mul_f32 v[118:119], v[118:119], v[42:43]
	v_pk_fma_f32 v[130:131], v[130:131], s[0:1], v[152:153] op_sel_hi:[1,0,0]
	v_pk_mul_f32 v[124:125], v[124:125], v[40:41]
	v_mul_f32_e32 v132, 0x4b800000, v131
	v_cmp_gt_f32_e32 vcc, s1, v131
	v_pk_mul_f32 v[128:129], v[128:129], v[48:49]
	v_pk_mul_f32 v[116:117], v[116:117], v[36:37]
	v_pk_mul_f32 v[120:121], v[120:121], v[44:45]
	v_cndmask_b32_e32 v131, v131, v132, vcc
	v_mul_f32_e32 v132, 0x4b800000, v130
	v_cmp_gt_f32_e64 s[0:1], s1, v130
	v_pk_fma_f32 v[112:113], v[112:113], v[28:29], v[120:121]
	v_pk_fma_f32 v[104:105], v[104:105], v[20:21], v[116:117]
	v_pk_fma_f32 v[108:109], v[108:109], v[32:33], v[128:129]
	v_pk_fma_f32 v[100:101], v[100:101], v[24:25], v[124:125]
	v_pk_fma_f32 v[110:111], v[110:111], v[26:27], v[118:119]
	v_pk_fma_f32 v[102:103], v[102:103], v[18:19], v[114:115]
	v_pk_fma_f32 v[106:107], v[106:107], v[30:31], v[126:127]
	v_pk_fma_f32 v[98:99], v[98:99], v[22:23], v[122:123]
	v_rsq_f32_e32 v131, v131
	v_cndmask_b32_e64 v130, v130, v132, s[0:1]
	v_pk_add_f32 v[98:99], v[98:99], v[106:107]
	v_pk_add_f32 v[102:103], v[102:103], v[110:111]
	v_pk_add_f32 v[100:101], v[100:101], v[108:109]
	v_pk_add_f32 v[104:105], v[104:105], v[112:113]
	v_rsq_f32_e32 v132, v130
	v_pk_add_f32 v[100:101], v[104:105], v[100:101]
	v_pk_add_f32 v[98:99], v[102:103], v[98:99]
	v_mul_f32_e32 v130, 0x45800000, v131
	v_add_f32_e32 v98, v98, v99
	v_add_f32_e32 v99, v100, v101
	v_add_f32_e32 v98, v98, v99
	v_mov_b32_e32 v99, v98
	v_pk_mul_f32 v[90:91], v[90:91], v[38:39]
	v_pk_mul_f32 v[94:95], v[94:95], v[46:47]
	v_pk_mul_f32 v[82:83], v[82:83], v[34:35]
	v_pk_mul_f32 v[86:87], v[86:87], v[42:43]
	v_cndmask_b32_e32 v130, v131, v130, vcc
	v_mul_f32_e32 v131, 0x45800000, v132
	v_permlane32_swap_b32_e32 v98, v99
	v_pk_fma_f32 v[78:79], v[78:79], v[26:27], v[86:87]
	v_pk_fma_f32 v[70:71], v[70:71], v[18:19], v[82:83]
	v_pk_fma_f32 v[74:75], v[74:75], v[30:31], v[94:95]
	v_pk_fma_f32 v[66:67], v[66:67], v[22:23], v[90:91]
	v_cndmask_b32_e64 v131, v132, v131, s[0:1]
	v_add_f32_e32 v98, v98, v99
	v_pk_add_f32 v[66:67], v[66:67], v[74:75]
	v_pk_add_f32 v[70:71], v[70:71], v[78:79]
	v_mul_f32_e32 v139, v160, v130
	v_mul_f32_e32 v98, v98, v131
	v_pk_add_f32 v[66:67], v[70:71], v[66:67]
	v_cmp_gt_u32_e32 vcc, 32, v1
	v_add_f32_e32 v66, v66, v67
	v_pk_mul_f32 v[92:93], v[92:93], v[40:41]
	v_cndmask_b32_e32 v67, v98, v139, vcc
	v_add_f32_e32 v67, s12, v67
	v_pk_mul_f32 v[96:97], v[96:97], v[48:49]
	v_pk_mul_f32 v[84:85], v[84:85], v[36:37]
	v_pk_mul_f32 v[88:89], v[88:89], v[44:45]
	v_mul_f32_e32 v67, 0xbfb8aa3b, v67
	v_pk_fma_f32 v[80:81], v[80:81], v[28:29], v[88:89]
	v_pk_fma_f32 v[72:73], v[72:73], v[20:21], v[84:85]
	v_pk_fma_f32 v[76:77], v[76:77], v[32:33], v[96:97]
	v_pk_fma_f32 v[68:69], v[68:69], v[24:25], v[92:93]
	v_exp_f32_e32 v70, v67
	v_pk_add_f32 v[68:69], v[68:69], v[76:77]
	v_pk_add_f32 v[72:73], v[72:73], v[80:81]
	v_cmp_lt_i32_e64 s[0:1], 0, v151
	v_pk_add_f32 v[68:69], v[72:73], v[68:69]
	v_mov_b32_e32 v137, v136
	v_add_f32_e32 v67, v68, v69
	v_add_f32_e32 v67, v66, v67
	v_add_f32_e32 v66, 1.0, v70
	v_rcp_f32_e32 v66, v66
	v_mov_b32_e32 v69, 0xff800000
	v_mov_b32_e32 v138, v133
	v_mov_b32_e32 v68, v67
	v_cndmask_b32_e64 v70, v69, v66, s[0:1]
	v_mbcnt_lo_u32_b32 v66, -1, 0
	v_mbcnt_hi_u32_b32 v66, -1, v66
	v_permlane32_swap_b32_e32 v136, v137
	v_permlane32_swap_b32_e32 v133, v138
	v_permlane32_swap_b32_e32 v67, v68
	v_and_b32_e32 v86, 64, v66
	s_mov_b32 s14, 8
	s_mov_b32 s13, 0
	v_mov_b32_e32 v66, 0
	s_waitcnt lgkmcnt(0)
